# v46 + dead zero-fills of the conversion hooks' load destinations removed (column-bound predicate is always true for these shapes)
# speedup vs baseline: 1.0126x; 1.0038x over previous
; #define GAS __attribute__((address_space(1)))
; __device__ __forceinline__ void conv_load(const float* W, int N, int k0, int n0, int wave, int lane, f32x4 (&r)[8]) {
;     const int n = n0 + 4 * lane; const bool ok = n < N;
;     const float* p = W + (size_t)(k0 + 8 * wave) * N + n;
; #pragma unroll
;     for (int i = 0; i < 8; ++i) r[i] = ok ? __builtin_nontemporal_load((const GAS f32x4*)(p + (size_t)i * N)) : (f32x4){0.f, 0.f, 0.f, 0.f};
; __device__ __forceinline__ bool conv_decode_moe(KA A, int t, ConvTile& c) {
;     unsigned char* ws = A->ws; c.f8 = 1; c.K = D; c.N = FFE; t -= 4096;
;     if (t < 14336) { const int hf = t / 7168, r2 = t % 7168, e = r2 / 896, r = r2 % 896, hk = r & 1, q = r >> 1; c.W = (hf ? A->in[I_MWU] : A->in[I_MWG]) + (size_t)e * D * FFE; c.WT = ws + WS_MUP + (size_t)e * 2 * FFE * D; c.k0 = 128 * (q / 28) + 64 * hk; c.n0 = 256 * (q % 28); c.kind = 2 + hf; return true; } t -= 14336;
;     if (t >= 7168) return false;
;     { const int e = t / 896, r = t % 896, hk = r & 1, q = r >> 1; c.W = A->in[I_MWD] + (size_t)e * FFE * D; c.WT = ws + WS_MDN + (size_t)e * D * FFE; c.K = FFE; c.N = D; c.k0 = 128 * (q >> 3) + 64 * hk; c.n0 = 256 * (q & 7); c.kind = 0; return true; }
.LBB0_766:
	v_mov_b32_e32 v29, 0
	s_and_b64 vcc, exec, s[12:13]
	v_mov_b32_e32 v28, v29
	v_mov_b32_e32 v27, v29
	v_mov_b32_e32 v26, v29
	v_mov_b32_e32 v33, v29
	v_mov_b32_e32 v32, v29
	v_mov_b32_e32 v31, v29
	v_mov_b32_e32 v30, v29
	v_mov_b32_e32 v25, v29
	v_mov_b32_e32 v24, v29
	v_mov_b32_e32 v23, v29
	v_mov_b32_e32 v22, v29
	v_mov_b32_e32 v21, v29
	v_mov_b32_e32 v20, v29
	v_mov_b32_e32 v19, v29
	v_mov_b32_e32 v18, v29
	v_mov_b32_e32 v17, v29
	v_mov_b32_e32 v16, v29
	v_mov_b32_e32 v15, v29
	v_mov_b32_e32 v14, v29
	v_mov_b32_e32 v13, v29
	v_mov_b32_e32 v12, v29
	v_mov_b32_e32 v11, v29
	v_mov_b32_e32 v10, v29
	v_mov_b32_e32 v9, v29
	v_mov_b32_e32 v8, v29
	v_mov_b32_e32 v7, v29
	v_mov_b32_e32 v6, v29
	v_mov_b32_e32 v5, v29
	v_mov_b32_e32 v4, v29
	v_mov_b32_e32 v3, v29
	v_mov_b32_e32 v2, v29
	s_cbranch_vccz .LBB0_778
	s_add_u32 s6, s14, s6
	s_addc_u32 s7, s15, s7
	s_load_dwordx2 s[6:7], s[6:7], 0x0
	s_mul_hi_i32 s1, s4, 0x3800000
	s_mul_i32 s4, s4, 0x3800000
	v_or_b32_e32 v2, s11, v153
	v_ashrrev_i32_e32 v3, 31, v2
	s_waitcnt lgkmcnt(0)
	s_add_u32 s6, s6, s4
	s_addc_u32 s7, s7, s1
	s_lshl_b32 s1, s0, 3
	s_add_i32 s4, s10, s1
	s_mul_hi_i32 s5, s4, s2
	s_mul_i32 s4, s4, s2
	s_lshl_b64 s[4:5], s[4:5], 2
	s_add_u32 s4, s6, s4
	s_addc_u32 s5, s7, s5
	v_cmp_le_i32_e32 vcc, s2, v2
	v_cmp_gt_i32_e64 s[40:41], s2, v2
	v_lshl_add_u64 v[34:35], v[2:3], 2, s[4:5]
	v_mov_b32_e32 v2, 0
	s_and_saveexec_b64 s[4:5], s[40:41]
	s_cbranch_execz .LBB0_769
	s_lshl_b32 s24, s2, 2
	v_lshl_add_u64 v[6:7], v[34:35], 0, s[24:25]
	global_load_dwordx4 v[2:5], v[34:35], off nt
	s_nop 0
	global_load_dwordx4 v[6:9], v[6:7], off nt
.LBB0_769:
	s_or_b64 exec, exec, s[4:5]
	s_and_saveexec_b64 s[4:5], vcc
	s_xor_b64 s[4:5], exec, s[4:5]
	s_or_saveexec_b64 s[4:5], s[4:5]
	v_mov_b32_e32 v10, 0
	s_xor_b64 exec, exec, s[4:5]
	s_cbranch_execz .LBB0_771
	s_lshl_b32 s24, s2, 3
	v_lshl_add_u64 v[10:11], v[34:35], 0, s[24:25]
	s_lshl_b32 s24, s2, 2
	v_lshl_add_u64 v[14:15], v[10:11], 0, s[24:25]
	global_load_dwordx4 v[10:13], v[10:11], off nt
	s_nop 0
	global_load_dwordx4 v[14:17], v[14:15], off nt
.LBB0_771:
	s_or_b64 exec, exec, s[4:5]
	s_and_saveexec_b64 s[4:5], vcc
	s_xor_b64 s[4:5], exec, s[4:5]
	s_or_saveexec_b64 s[4:5], s[4:5]
	v_mov_b32_e32 v18, 0
	s_xor_b64 exec, exec, s[4:5]
	s_cbranch_execz .LBB0_773
	s_lshl_b32 s24, s2, 4
	v_lshl_add_u64 v[18:19], v[34:35], 0, s[24:25]
	s_lshl_b32 s24, s2, 2
	v_lshl_add_u64 v[22:23], v[18:19], 0, s[24:25]
	global_load_dwordx4 v[18:21], v[18:19], off nt
	s_nop 0
	global_load_dwordx4 v[22:25], v[22:23], off nt
.LBB0_773:
	s_or_b64 exec, exec, s[4:5]
	s_and_saveexec_b64 s[4:5], vcc
	s_xor_b64 s[4:5], exec, s[4:5]
	s_or_saveexec_b64 s[4:5], s[4:5]
	s_xor_b64 exec, exec, s[4:5]
	s_cbranch_execz .LBB0_777
	s_mul_i32 s24, s2, 24
	v_lshl_add_u64 v[26:27], v[34:35], 0, s[24:25]
	s_lshl_b32 s24, s2, 2
	v_lshl_add_u64 v[28:29], v[26:27], 0, s[24:25]
	global_load_dwordx4 v[30:33], v[26:27], off nt
	s_nop 0
	global_load_dwordx4 v[26:29], v[28:29], off nt

; #define GAS __attribute__((address_space(1)))
; #define CV_LOAD(j, R) do { ConvTile c_; if (CV_VALID(j) && CV_DEC(CV_TILE(j), c_)) conv_load(c_.W, c_.N, c_.k0, c_.n0, wave, lane, R); } while (0)
; #define CV_PROC(j, R) { ConvTile c_; if (!CV_VALID(j) || !CV_DEC(CV_TILE(j), c_)) break; if constexpr (MOE) conv_emit_moe(c_, R, T, tid, wave, lane); else conv_emit(c_, R, T, tid, wave, lane); }
; __device__ __forceinline__ void conv_load(const float* W, int N, int k0, int n0, int wave, int lane, f32x4 (&r)[8]) {
;     const int n = n0 + 4 * lane; const bool ok = n < N;
;     const float* p = W + (size_t)(k0 + 8 * wave) * N + n;
; #pragma unroll
;     for (int i = 0; i < 8; ++i) r[i] = ok ? __builtin_nontemporal_load((const GAS f32x4*)(p + (size_t)i * N)) : (f32x4){0.f, 0.f, 0.f, 0.f};
; template <int NSLOT, bool MOE> __device__ __forceinline__ void conv_burst(const ConvHook& h, int bid, PG8_LAS unsigned char* T_, int tid) {
;     ...
;         CV_LOAD(0, R0); CV_LOAD(1, R1); CV_LOAD(2, R2);
;         for (int j = 0;; j += 4) {
;             CV_LOAD(j + 3, R3); CV_PROC(j, R0)
.LBB0_784:
	s_or_b64 exec, exec, s[4:5]
	s_and_saveexec_b64 s[4:5], s[38:39]
	s_cbranch_execz .LBB0_786
	v_readlane_b32 s6, v255, 12
	v_readlane_b32 s7, v255, 13
	s_nop 1
	v_lshl_add_u64 v[58:59], v[66:67], 0, s[6:7]
	v_readlane_b32 s6, v255, 15
	v_readlane_b32 s7, v255, 16
	s_nop 1
	v_lshl_add_u64 v[60:61], v[58:59], 0, s[6:7]
	global_load_dwordx4 v[62:65], v[58:59], off nt
	s_nop 0
	global_load_dwordx4 v[58:61], v[60:61], off nt

; #define GAS __attribute__((address_space(1)))
; #define CV_LOAD(j, R) do { ConvTile c_; if (CV_VALID(j) && CV_DEC(CV_TILE(j), c_)) conv_load(c_.W, c_.N, c_.k0, c_.n0, wave, lane, R); } while (0)
; #define CV_PROC(j, R) { ConvTile c_; if (!CV_VALID(j) || !CV_DEC(CV_TILE(j), c_)) break; if constexpr (MOE) conv_emit_moe(c_, R, T, tid, wave, lane); else conv_emit(c_, R, T, tid, wave, lane); }
; __device__ __forceinline__ void conv_load(const float* W, int N, int k0, int n0, int wave, int lane, f32x4 (&r)[8]) {
;     const int n = n0 + 4 * lane; const bool ok = n < N;
;     const float* p = W + (size_t)(k0 + 8 * wave) * N + n;
; #pragma unroll
;     for (int i = 0; i < 8; ++i) r[i] = ok ? __builtin_nontemporal_load((const GAS f32x4*)(p + (size_t)i * N)) : (f32x4){0.f, 0.f, 0.f, 0.f};
; template <int NSLOT, bool MOE> __device__ __forceinline__ void conv_burst(const ConvHook& h, int bid, PG8_LAS unsigned char* T_, int tid) {
;     ...
;         CV_LOAD(0, R0); CV_LOAD(1, R1); CV_LOAD(2, R2);
;         for (int j = 0;; j += 4) {
;             CV_LOAD(j + 3, R3); CV_PROC(j, R0)
.LBB0_797:
	s_or_b64 exec, exec, s[4:5]
	s_and_saveexec_b64 s[4:5], vcc
	s_cbranch_execz .LBB0_799
	s_mul_i32 s24, s1, 24
	v_lshl_add_u64 v[90:91], v[98:99], 0, s[24:25]
	s_lshl_b32 s24, s1, 2
	v_lshl_add_u64 v[92:93], v[90:91], 0, s[24:25]
	global_load_dwordx4 v[94:97], v[90:91], off nt
	s_nop 0
	global_load_dwordx4 v[90:93], v[92:93], off nt

; #define GAS __attribute__((address_space(1)))
; #define CV_LOAD(j, R) do { ConvTile c_; if (CV_VALID(j) && CV_DEC(CV_TILE(j), c_)) conv_load(c_.W, c_.N, c_.k0, c_.n0, wave, lane, R); } while (0)
; #define CV_PROC(j, R) { ConvTile c_; if (!CV_VALID(j) || !CV_DEC(CV_TILE(j), c_)) break; if constexpr (MOE) conv_emit_moe(c_, R, T, tid, wave, lane); else conv_emit(c_, R, T, tid, wave, lane); }
; __device__ __forceinline__ void conv_load(const float* W, int N, int k0, int n0, int wave, int lane, f32x4 (&r)[8]) {
;     const int n = n0 + 4 * lane; const bool ok = n < N;
;     const float* p = W + (size_t)(k0 + 8 * wave) * N + n;
; #pragma unroll
;     for (int i = 0; i < 8; ++i) r[i] = ok ? __builtin_nontemporal_load((const GAS f32x4*)(p + (size_t)i * N)) : (f32x4){0.f, 0.f, 0.f, 0.f};
; template <int NSLOT, bool MOE> __device__ __forceinline__ void conv_burst(const ConvHook& h, int bid, PG8_LAS unsigned char* T_, int tid) {
;     ...
;             CV_LOAD(j + 3, R3); CV_PROC(j, R0)
.Lhw_fast_1:
.Lhw_done_1:
	v_add_u32_e32 v98, s42, v153
	s_add_u32 s4, s84, s4
	s_addc_u32 s5, s85, s5
	v_ashrrev_i32_e32 v99, 31, v98
	v_cmp_gt_i32_e32 vcc, s24, v98
	v_lshl_add_u64 v[132:133], v[98:99], 2, s[4:5]
	s_and_saveexec_b64 s[4:5], vcc
	s_cbranch_execz .LBB0_814
	v_lshl_add_u64 v[100:101], s[24:25], 2, v[132:133]
	global_load_dwordx4 v[102:105], v[132:133], off nt
	global_load_dwordx4 v[106:109], v[100:101], off nt
.LBB0_814:
	s_or_b64 exec, exec, s[4:5]
	s_and_saveexec_b64 s[4:5], vcc
	s_cbranch_execz .LBB0_816
	v_lshl_add_u64 v[98:99], s[24:25], 3, v[132:133]
	v_lshl_add_u64 v[110:111], s[24:25], 2, v[98:99]
	global_load_dwordx4 v[98:101], v[98:99], off nt
	s_nop 0
	global_load_dwordx4 v[110:113], v[110:111], off nt
.LBB0_816:
	s_or_b64 exec, exec, s[4:5]
	s_and_saveexec_b64 s[4:5], vcc
	s_cbranch_execz .LBB0_818
	v_lshl_add_u64 v[114:115], s[24:25], 4, v[132:133]
	v_lshl_add_u64 v[118:119], s[24:25], 2, v[114:115]
	global_load_dwordx4 v[114:117], v[114:115], off nt
	s_nop 0
	global_load_dwordx4 v[118:121], v[118:119], off nt
.LBB0_818:
	s_or_b64 exec, exec, s[4:5]
	s_and_saveexec_b64 s[4:5], vcc
	s_cbranch_execz .LBB0_820
	s_mul_i32 s6, s24, 24
	s_mov_b32 s7, s25
	v_lshl_add_u64 v[122:123], v[132:133], 0, s[6:7]
	v_lshl_add_u64 v[124:125], s[24:25], 2, v[122:123]
	global_load_dwordx4 v[126:129], v[122:123], off nt
	s_nop 0
	global_load_dwordx4 v[122:125], v[124:125], off nt

; #define GAS __attribute__((address_space(1)))
; #define CV_LOAD(j, R) do { ConvTile c_; if (CV_VALID(j) && CV_DEC(CV_TILE(j), c_)) conv_load(c_.W, c_.N, c_.k0, c_.n0, wave, lane, R); } while (0)
; #define CV_PROC(j, R) { ConvTile c_; if (!CV_VALID(j) || !CV_DEC(CV_TILE(j), c_)) break; if constexpr (MOE) conv_emit_moe(c_, R, T, tid, wave, lane); else conv_emit(c_, R, T, tid, wave, lane); }
; __device__ __forceinline__ void conv_load(const float* W, int N, int k0, int n0, int wave, int lane, f32x4 (&r)[8]) {
;     const int n = n0 + 4 * lane; const bool ok = n < N;
;     const float* p = W + (size_t)(k0 + 8 * wave) * N + n;
; #pragma unroll
;     for (int i = 0; i < 8; ++i) r[i] = ok ? __builtin_nontemporal_load((const GAS f32x4*)(p + (size_t)i * N)) : (f32x4){0.f, 0.f, 0.f, 0.f};
; template <int NSLOT, bool MOE> __device__ __forceinline__ void conv_burst(const ConvHook& h, int bid, PG8_LAS unsigned char* T_, int tid) {
;     ...
;             CV_LOAD(j + 4, R0); CV_PROC(j + 1, R1)
.LBB0_846:
	s_andn2_b64 vcc, exec, s[12:13]
	s_cbranch_vccnz .LBB0_858
	s_add_i32 s6, s43, s53
	s_ashr_i32 s7, s6, 31
	s_mul_i32 s7, s7, s24
	s_mul_hi_u32 s12, s6, s24
	s_add_i32 s7, s12, s7
	s_mul_i32 s6, s6, s24
	v_add_u32_e32 v2, s16, v153
	s_lshl_b64 s[6:7], s[6:7], 2
	v_cmp_le_i32_e32 vcc, s24, v2
	s_add_u32 s12, s88, s6
	s_addc_u32 s13, s89, s7
	s_and_saveexec_b64 s[6:7], vcc
	s_xor_b64 s[6:7], exec, s[6:7]
	s_or_saveexec_b64 s[6:7], s[6:7]
	v_ashrrev_i32_e32 v3, 31, v2
	v_lshl_add_u64 v[132:133], v[2:3], 2, s[12:13]
	s_xor_b64 exec, exec, s[6:7]
	s_cbranch_execz .LBB0_849
	v_lshl_add_u64 v[6:7], s[24:25], 2, v[132:133]
	global_load_dwordx4 v[2:5], v[132:133], off nt
	s_nop 0
	global_load_dwordx4 v[6:9], v[6:7], off nt
.LBB0_849:
	s_or_b64 exec, exec, s[6:7]
	s_and_saveexec_b64 s[6:7], vcc
	s_xor_b64 s[6:7], exec, s[6:7]
	s_or_saveexec_b64 s[6:7], s[6:7]
	s_xor_b64 exec, exec, s[6:7]
	s_cbranch_execz .LBB0_851
	v_lshl_add_u64 v[10:11], s[24:25], 3, v[132:133]
	v_lshl_add_u64 v[14:15], s[24:25], 2, v[10:11]
	global_load_dwordx4 v[10:13], v[10:11], off nt
	s_nop 0
	global_load_dwordx4 v[14:17], v[14:15], off nt
.LBB0_851:
	s_or_b64 exec, exec, s[6:7]
	s_and_saveexec_b64 s[6:7], vcc
	s_xor_b64 s[6:7], exec, s[6:7]
	s_or_saveexec_b64 s[6:7], s[6:7]
	s_xor_b64 exec, exec, s[6:7]
	s_cbranch_execz .LBB0_853
	v_lshl_add_u64 v[18:19], s[24:25], 4, v[132:133]
	v_lshl_add_u64 v[22:23], s[24:25], 2, v[18:19]
	global_load_dwordx4 v[18:21], v[18:19], off nt
	s_nop 0
	global_load_dwordx4 v[22:25], v[22:23], off nt
.LBB0_853:
	s_or_b64 exec, exec, s[6:7]
	s_and_saveexec_b64 s[6:7], vcc
	s_xor_b64 s[6:7], exec, s[6:7]
	s_or_saveexec_b64 s[6:7], s[6:7]
	s_xor_b64 exec, exec, s[6:7]
	s_cbranch_execz .LBB0_857
	s_mul_i32 s12, s24, 24
	s_mov_b32 s13, s25
	v_lshl_add_u64 v[26:27], v[132:133], 0, s[12:13]
	v_lshl_add_u64 v[28:29], s[24:25], 2, v[26:27]
	global_load_dwordx4 v[30:33], v[26:27], off nt
	s_nop 0
	global_load_dwordx4 v[26:29], v[28:29], off nt

; #define GAS __attribute__((address_space(1)))
; #define CV_LOAD(j, R) do { ConvTile c_; if (CV_VALID(j) && CV_DEC(CV_TILE(j), c_)) conv_load(c_.W, c_.N, c_.k0, c_.n0, wave, lane, R); } while (0)
; #define CV_PROC(j, R) { ConvTile c_; if (!CV_VALID(j) || !CV_DEC(CV_TILE(j), c_)) break; if constexpr (MOE) conv_emit_moe(c_, R, T, tid, wave, lane); else conv_emit(c_, R, T, tid, wave, lane); }
; __device__ __forceinline__ void conv_load(const float* W, int N, int k0, int n0, int wave, int lane, f32x4 (&r)[8]) {
;     const int n = n0 + 4 * lane; const bool ok = n < N;
;     const float* p = W + (size_t)(k0 + 8 * wave) * N + n;
; #pragma unroll
;     for (int i = 0; i < 8; ++i) r[i] = ok ? __builtin_nontemporal_load((const GAS f32x4*)(p + (size_t)i * N)) : (f32x4){0.f, 0.f, 0.f, 0.f};
; template <int NSLOT, bool MOE> __device__ __forceinline__ void conv_burst(const ConvHook& h, int bid, PG8_LAS unsigned char* T_, int tid) {
;     ...
;             CV_LOAD(j + 5, R1); CV_PROC(j + 2, R2)
.LBB0_889:
	s_or_b64 exec, exec, s[6:7]
	s_and_saveexec_b64 s[6:7], vcc
	s_cbranch_execz .LBB0_891
	s_mul_i32 s12, s24, 24
	s_mov_b32 s13, s25
	v_lshl_add_u64 v[58:59], v[148:149], 0, s[12:13]
	v_lshl_add_u64 v[60:61], s[24:25], 2, v[58:59]
	global_load_dwordx4 v[62:65], v[58:59], off nt
	s_nop 0
	global_load_dwordx4 v[58:61], v[60:61], off nt

; #define GAS __attribute__((address_space(1)))
; #define CV_LOAD(j, R) do { ConvTile c_; if (CV_VALID(j) && CV_DEC(CV_TILE(j), c_)) conv_load(c_.W, c_.N, c_.k0, c_.n0, wave, lane, R); } while (0)
; #define CV_PROC(j, R) { ConvTile c_; if (!CV_VALID(j) || !CV_DEC(CV_TILE(j), c_)) break; if constexpr (MOE) conv_emit_moe(c_, R, T, tid, wave, lane); else conv_emit(c_, R, T, tid, wave, lane); }
; __device__ __forceinline__ void conv_load(const float* W, int N, int k0, int n0, int wave, int lane, f32x4 (&r)[8]) {
;     const int n = n0 + 4 * lane; const bool ok = n < N;
;     const float* p = W + (size_t)(k0 + 8 * wave) * N + n;
; #pragma unroll
;     for (int i = 0; i < 8; ++i) r[i] = ok ? __builtin_nontemporal_load((const GAS f32x4*)(p + (size_t)i * N)) : (f32x4){0.f, 0.f, 0.f, 0.f};
; template <int NSLOT, bool MOE> __device__ __forceinline__ void conv_burst(const ConvHook& h, int bid, PG8_LAS unsigned char* T_, int tid) {
;     ...
;             CV_LOAD(j + 6, R2); CV_PROC(j + 3, R3)
.LBB0_923:
	s_or_b64 exec, exec, s[6:7]
	s_and_saveexec_b64 s[6:7], vcc
	s_cbranch_execz .LBB0_925
	s_mul_i32 s12, s24, 24
	s_mov_b32 s13, s25
	v_lshl_add_u64 v[90:91], v[148:149], 0, s[12:13]
	v_lshl_add_u64 v[92:93], s[24:25], 2, v[90:91]
	global_load_dwordx4 v[94:97], v[90:91], off nt
	s_nop 0
	global_load_dwordx4 v[90:93], v[92:93], off nt

; __device__ __forceinline__ unsigned cvt_pk_bf16(float lo, float hi) { unsigned r; asm volatile("v_cvt_pk_bf16_f32 %0, %1, %2" : "=v"(r) : "v"(lo), "v"(hi)); return r; }
;     __device__ __forceinline__ void operator()(const f32x4 (&acc)[2][2][4][2], const Unit& u, int wr, int wc, int fr, int fq) const {
;         const int pl = u.pn % nt; const int row0 = u.pm * BM + wr * 64 + fr, col0 = pl * HALF + wc * 32 + 8 * fq;
; #pragma unroll
;         for (int ai = 0; ai < 2; ++ai)
; #pragma unroll
;             for (int m = 0; m < 4; ++m) { bf16_t* rowp = O + (size_t)(row0 + ai * HALF + m * 16) * ldc + col0;
;                 float a[8];
; #pragma unroll
;                 for (int n = 0; n < 2; ++n)
; #pragma unroll
;                     for (int e = 0; e < 4; e += 2) { typedef float f32x2 __attribute__((ext_vector_type(2)));
;                         const f32x2 g = {acc[ai][0][m][n][e], acc[ai][0][m][n][e + 1]}, up = {acc[ai][1][m][n][e], acc[ai][1][m][n][e + 1]};
;                         const f32x2 x = g * (f32x2){-1.44269504f, -1.44269504f};
;                         const f32x2 d = (f32x2){__builtin_amdgcn_exp2f(x.x), __builtin_amdgcn_exp2f(x.y)} + (f32x2){1.f, 1.f};
;                         const f32x2 o = (g * up) * (f32x2){__builtin_amdgcn_rcpf(d.x), __builtin_amdgcn_rcpf(d.y)};
;                         a[4 * n + e] = o.x; a[4 * n + e + 1] = o.y; }
;                 u32x4 w; w.x = cvt_pk_bf16(a[0], a[1]); w.y = cvt_pk_bf16(a[2], a[3]); w.z = cvt_pk_bf16(a[4], a[5]); w.w = cvt_pk_bf16(a[6], a[7]);
;                 *(u32x4*)rowp = w; }
.LBB0_2285:
	s_mul_hi_i32 s5, s4, 0x2e8ba2e9
	s_lshr_b32 s6, s5, 31
	s_lshr_b32 s5, s5, 3
	s_add_i32 s5, s5, s6
	s_mov_b32 s6, 0xbfb8aa3b
	v_pk_mul_f32 v[172:173], v[122:123], s[6:7] op_sel_hi:[1,0]
	v_pk_mul_f32 v[122:123], v[122:123], v[126:127]
	v_exp_f32_e32 v172, v172
	v_exp_f32_e32 v173, v173
	v_pk_mul_f32 v[128:129], v[124:125], v[128:129]
	v_pk_mul_f32 v[124:125], v[124:125], s[6:7] op_sel_hi:[1,0]
	s_mul_i32 s5, s5, 44
	v_pk_add_f32 v[172:173], v[172:173], 1.0 op_sel_hi:[1,0]
	v_exp_f32_e32 v124, v124
	v_rcp_f32_e32 v126, v172
	v_rcp_f32_e32 v127, v173
	v_exp_f32_e32 v125, v125
	s_sub_i32 s4, s4, s5
	v_lshl_or_b32 v152, s4, 7, v169
	v_pk_mul_f32 v[122:123], v[126:127], v[122:123]
	v_pk_mul_f32 v[126:127], v[114:115], s[6:7] op_sel_hi:[1,0]
	v_pk_mul_f32 v[114:115], v[114:115], v[118:119]
	v_exp_f32_e32 v126, v126
	v_exp_f32_e32 v127, v127
	v_pk_add_f32 v[124:125], v[124:125], 1.0 op_sel_hi:[1,0]
	v_lshl_add_u32 v131, s14, 8, v155
	v_rcp_f32_e32 v124, v124
	v_pk_add_f32 v[126:127], v[126:127], 1.0 op_sel_hi:[1,0]
	v_rcp_f32_e32 v125, v125
	v_rcp_f32_e32 v118, v126
	v_rcp_f32_e32 v119, v127
	v_ashrrev_i32_e32 v153, 31, v152
	v_mov_b64_e32 v[132:133], s[8:9]
	v_pk_mul_f32 v[120:121], v[116:117], v[120:121]
	v_pk_mul_f32 v[118:119], v[118:119], v[114:115]
	v_pk_mul_f32 v[114:115], v[116:117], s[6:7] op_sel_hi:[1,0]
	v_mad_i64_i32 v[158:159], s[4:5], v131, s66, v[132:133]
	v_exp_f32_e32 v114, v114
	v_exp_f32_e32 v115, v115
	v_pk_mul_f32 v[124:125], v[124:125], v[128:129]
	v_cvt_pk_bf16_f32 v116, v122, v123
	v_pk_mul_f32 v[112:113], v[108:109], v[112:113]
	v_pk_add_f32 v[114:115], v[114:115], 1.0 op_sel_hi:[1,0]
	v_cvt_pk_bf16_f32 v117, v124, v125
	v_cvt_pk_bf16_f32 v118, v118, v119
	v_pk_mul_f32 v[108:109], v[108:109], s[6:7] op_sel_hi:[1,0]
	v_rcp_f32_e32 v114, v114
	v_rcp_f32_e32 v115, v115
	v_exp_f32_e32 v108, v108
	v_exp_f32_e32 v109, v109
	v_pk_mul_f32 v[104:105], v[100:101], v[104:105]
	v_pk_mul_f32 v[120:121], v[114:115], v[120:121]
	v_lshlrev_b64 v[114:115], 1, v[152:153]
	v_lshl_add_u64 v[126:127], v[158:159], 0, v[114:115]
	v_cvt_pk_bf16_f32 v119, v120, v121
	global_store_dwordx4 v[126:127], v[116:119], off
	v_pk_add_f32 v[108:109], v[108:109], 1.0 op_sel_hi:[1,0]
	v_pk_mul_f32 v[96:97], v[92:93], v[96:97]
	v_pk_mul_f32 v[118:119], v[106:107], s[6:7] op_sel_hi:[1,0]
	v_pk_mul_f32 v[106:107], v[106:107], v[110:111]
	v_exp_f32_e32 v118, v118
	v_exp_f32_e32 v119, v119
	v_rcp_f32_e32 v108, v108
	v_rcp_f32_e32 v109, v109
	v_or_b32_e32 v116, 16, v131
	v_pk_add_f32 v[118:119], v[118:119], 1.0 op_sel_hi:[1,0]
	v_mad_i64_i32 v[116:117], s[4:5], v116, s66, v[132:133]
	v_rcp_f32_e32 v110, v118
	v_rcp_f32_e32 v111, v119
	v_pk_mul_f32 v[108:109], v[108:109], v[112:113]
	v_pk_mul_f32 v[92:93], v[92:93], s[6:7] op_sel_hi:[1,0]
	v_pk_mul_f32 v[88:89], v[84:85], v[88:89]
	v_pk_mul_f32 v[106:107], v[110:111], v[106:107]
	v_pk_mul_f32 v[110:111], v[98:99], s[6:7] op_sel_hi:[1,0]
	v_pk_mul_f32 v[98:99], v[98:99], v[102:103]
	v_exp_f32_e32 v110, v110
	v_exp_f32_e32 v111, v111
	v_exp_f32_e32 v92, v92
	v_exp_f32_e32 v93, v93
	v_pk_mul_f32 v[80:81], v[76:77], v[80:81]
	v_pk_add_f32 v[110:111], v[110:111], 1.0 op_sel_hi:[1,0]
	v_pk_mul_f32 v[76:77], v[76:77], s[6:7] op_sel_hi:[1,0]
	v_rcp_f32_e32 v102, v110
	v_rcp_f32_e32 v103, v111
	v_lshl_add_u64 v[110:111], v[116:117], 0, v[114:115]
	v_pk_add_f32 v[92:93], v[92:93], 1.0 op_sel_hi:[1,0]
	v_exp_f32_e32 v76, v76
	v_pk_mul_f32 v[102:103], v[102:103], v[98:99]
	v_pk_mul_f32 v[98:99], v[100:101], s[6:7] op_sel_hi:[1,0]
	v_rcp_f32_e32 v92, v92
	v_exp_f32_e32 v98, v98
	v_exp_f32_e32 v99, v99
	v_rcp_f32_e32 v93, v93
	v_exp_f32_e32 v77, v77
	v_pk_mul_f32 v[72:73], v[68:69], v[72:73]
	v_pk_add_f32 v[98:99], v[98:99], 1.0 op_sel_hi:[1,0]
	v_pk_mul_f32 v[92:93], v[92:93], v[96:97]
	v_rcp_f32_e32 v98, v98
	v_rcp_f32_e32 v99, v99
	v_pk_add_f32 v[76:77], v[76:77], 1.0 op_sel_hi:[1,0]
	v_pk_mul_f32 v[64:65], v[60:61], v[64:65]
	v_rcp_f32_e32 v76, v76
	v_pk_mul_f32 v[104:105], v[98:99], v[104:105]
	v_cvt_pk_bf16_f32 v98, v106, v107
	v_cvt_pk_bf16_f32 v99, v108, v109
	v_cvt_pk_bf16_f32 v100, v102, v103
	v_rcp_f32_e32 v77, v77
	v_cvt_pk_bf16_f32 v101, v104, v105
	global_store_dwordx4 v[110:111], v[98:101], off
	v_pk_mul_f32 v[60:61], v[60:61], s[6:7] op_sel_hi:[1,0]
	v_pk_mul_f32 v[76:77], v[76:77], v[80:81]
	v_pk_mul_f32 v[100:101], v[90:91], s[6:7] op_sel_hi:[1,0]
	v_pk_mul_f32 v[90:91], v[90:91], v[94:95]
	v_exp_f32_e32 v100, v100
	v_exp_f32_e32 v101, v101
	v_or_b32_e32 v98, 32, v131
	v_mad_i64_i32 v[98:99], s[4:5], v98, s66, v[132:133]
	v_pk_add_f32 v[100:101], v[100:101], 1.0 op_sel_hi:[1,0]
	v_exp_f32_e32 v60, v60
	v_rcp_f32_e32 v94, v100
	v_rcp_f32_e32 v95, v101
	v_exp_f32_e32 v61, v61
	v_pk_mul_f32 v[56:57], v[52:53], v[56:57]
	v_pk_mul_f32 v[48:49], v[44:45], v[48:49]
	v_pk_mul_f32 v[90:91], v[94:95], v[90:91]
	v_pk_mul_f32 v[94:95], v[82:83], s[6:7] op_sel_hi:[1,0]
	v_pk_mul_f32 v[82:83], v[82:83], v[86:87]
	v_exp_f32_e32 v94, v94
	v_exp_f32_e32 v95, v95
	v_pk_add_f32 v[60:61], v[60:61], 1.0 op_sel_hi:[1,0]
	v_pk_mul_f32 v[44:45], v[44:45], s[6:7] op_sel_hi:[1,0]
	v_rcp_f32_e32 v60, v60
	v_pk_add_f32 v[94:95], v[94:95], 1.0 op_sel_hi:[1,0]
	v_rcp_f32_e32 v61, v61
	v_rcp_f32_e32 v86, v94
	v_rcp_f32_e32 v87, v95
	v_lshl_add_u64 v[94:95], v[98:99], 0, v[114:115]
	v_pk_mul_f32 v[60:61], v[60:61], v[64:65]
	v_exp_f32_e32 v44, v44
	v_pk_mul_f32 v[86:87], v[86:87], v[82:83]
	v_pk_mul_f32 v[82:83], v[84:85], s[6:7] op_sel_hi:[1,0]
	v_exp_f32_e32 v45, v45
	v_exp_f32_e32 v82, v82
	v_exp_f32_e32 v83, v83
	v_pk_mul_f32 v[40:41], v[36:37], v[40:41]
	v_pk_add_f32 v[44:45], v[44:45], 1.0 op_sel_hi:[1,0]
; #define PG8_LAS __attribute__((address_space(3)))
; __device__ __forceinline__ unsigned cvt_pk_bf16(float lo, float hi) { unsigned r; asm volatile("v_cvt_pk_bf16_f32 %0, %1, %2" : "=v"(r) : "v"(lo), "v"(hi)); return r; }
;     __device__ __forceinline__ void done(const Unit&, int ui, PG8_LAS unsigned char* lds, int tid) const { if constexpr (HOOK) { if (ui == cv.trig) conv_burst<4, true>(cv, c, lds + 131072, tid); } }
;     __device__ __forceinline__ void done(const Unit&, int ui, PG8_LAS unsigned char* lds, int tid) const { if constexpr (HOOK) { if (ui == cv.trig) conv_burst<4, true>(cv, c, lds + 131072, tid); } }
;     __device__ __forceinline__ void operator()(const f32x4 (&acc)[2][2][4][2], const Unit& u, int wr, int wc, int fr, int fq) const {
;         const int pl = u.pn % nt; const int row0 = u.pm * BM + wr * 64 + fr, col0 = pl * HALF + wc * 32 + 8 * fq;
; #pragma unroll
;         for (int ai = 0; ai < 2; ++ai)
; #pragma unroll
;             for (int m = 0; m < 4; ++m) { bf16_t* rowp = O + (size_t)(row0 + ai * HALF + m * 16) * ldc + col0;
;                 float a[8];
; #pragma unroll
;                 for (int n = 0; n < 2; ++n)
; #pragma unroll
;                     for (int e = 0; e < 4; e += 2) { typedef float f32x2 __attribute__((ext_vector_type(2)));
;                         const f32x2 g = {acc[ai][0][m][n][e], acc[ai][0][m][n][e + 1]}, up = {acc[ai][1][m][n][e], acc[ai][1][m][n][e + 1]};
;                         const f32x2 x = g * (f32x2){-1.44269504f, -1.44269504f};
;                         const f32x2 d = (f32x2){__builtin_amdgcn_exp2f(x.x), __builtin_amdgcn_exp2f(x.y)} + (f32x2){1.f, 1.f};
;                         const f32x2 o = (g * up) * (f32x2){__builtin_amdgcn_rcpf(d.x), __builtin_amdgcn_rcpf(d.y)};
;                         a[4 * n + e] = o.x; a[4 * n + e + 1] = o.y; }
;                 u32x4 w; w.x = cvt_pk_bf16(a[0], a[1]); w.y = cvt_pk_bf16(a[2], a[3]); w.z = cvt_pk_bf16(a[4], a[5]); w.w = cvt_pk_bf16(a[6], a[7]);
;                 *(u32x4*)rowp = w; }
	v_pk_mul_f32 v[32:33], v[28:29], v[32:33]
	v_pk_add_f32 v[82:83], v[82:83], 1.0 op_sel_hi:[1,0]
	v_rcp_f32_e32 v44, v44
	v_rcp_f32_e32 v82, v82
	v_rcp_f32_e32 v83, v83
	v_rcp_f32_e32 v45, v45
	v_pk_mul_f32 v[28:29], v[28:29], s[6:7] op_sel_hi:[1,0]
	v_pk_mul_f32 v[24:25], v[20:21], v[24:25]
	v_pk_mul_f32 v[88:89], v[82:83], v[88:89]
	v_cvt_pk_bf16_f32 v82, v90, v91
	v_cvt_pk_bf16_f32 v83, v92, v93
	v_cvt_pk_bf16_f32 v84, v86, v87
	v_pk_mul_f32 v[44:45], v[44:45], v[48:49]
	v_cvt_pk_bf16_f32 v85, v88, v89
	global_store_dwordx4 v[94:95], v[82:85], off
	v_exp_f32_e32 v28, v28
	v_exp_f32_e32 v29, v29
	v_pk_mul_f32 v[84:85], v[74:75], s[6:7] op_sel_hi:[1,0]
	v_pk_mul_f32 v[74:75], v[74:75], v[78:79]
	v_exp_f32_e32 v84, v84
	v_exp_f32_e32 v85, v85
	v_or_b32_e32 v82, 48, v131
	v_mad_i64_i32 v[82:83], s[4:5], v82, s66, v[132:133]
	v_pk_add_f32 v[84:85], v[84:85], 1.0 op_sel_hi:[1,0]
	v_pk_add_f32 v[28:29], v[28:29], 1.0 op_sel_hi:[1,0]
	v_rcp_f32_e32 v78, v84
	v_rcp_f32_e32 v79, v85
	v_rcp_f32_e32 v28, v28
	v_rcp_f32_e32 v29, v29
	v_pk_mul_f32 v[16:17], v[12:13], v[16:17]
	v_pk_mul_f32 v[74:75], v[78:79], v[74:75]
	v_pk_mul_f32 v[78:79], v[66:67], s[6:7] op_sel_hi:[1,0]
	v_pk_mul_f32 v[66:67], v[66:67], v[70:71]
	v_exp_f32_e32 v78, v78
	v_exp_f32_e32 v79, v79
	v_pk_mul_f32 v[28:29], v[28:29], v[32:33]
	v_pk_mul_f32 v[12:13], v[12:13], s[6:7] op_sel_hi:[1,0]
	v_pk_mul_f32 v[8:9], v[4:5], v[8:9]
	v_pk_add_f32 v[78:79], v[78:79], 1.0 op_sel_hi:[1,0]
	v_exp_f32_e32 v12, v12
	v_rcp_f32_e32 v70, v78
	v_rcp_f32_e32 v71, v79
	v_lshl_add_u64 v[78:79], v[82:83], 0, v[114:115]
	v_exp_f32_e32 v13, v13
	s_cmp_lg_u32 s2, s71
	v_pk_mul_f32 v[70:71], v[70:71], v[66:67]
	v_pk_mul_f32 v[66:67], v[68:69], s[6:7] op_sel_hi:[1,0]
	v_pk_add_f32 v[12:13], v[12:13], 1.0 op_sel_hi:[1,0]
	v_exp_f32_e32 v66, v66
	v_exp_f32_e32 v67, v67
	v_rcp_f32_e32 v12, v12
	v_rcp_f32_e32 v13, v13
	v_pk_add_f32 v[66:67], v[66:67], 1.0 op_sel_hi:[1,0]
	s_nop 0
	v_rcp_f32_e32 v66, v66
	v_rcp_f32_e32 v67, v67
	v_pk_mul_f32 v[12:13], v[12:13], v[16:17]
	v_pk_mul_f32 v[72:73], v[66:67], v[72:73]
	v_cvt_pk_bf16_f32 v66, v74, v75
	v_cvt_pk_bf16_f32 v67, v76, v77
	v_cvt_pk_bf16_f32 v68, v70, v71
	s_nop 0
	v_cvt_pk_bf16_f32 v69, v72, v73
	global_store_dwordx4 v[78:79], v[66:69], off
	s_nop 1
	v_pk_mul_f32 v[68:69], v[58:59], s[6:7] op_sel_hi:[1,0]
	v_pk_mul_f32 v[58:59], v[58:59], v[62:63]
	v_exp_f32_e32 v68, v68
	v_exp_f32_e32 v69, v69
	v_add_u32_e32 v66, 0x80, v131
	v_mad_i64_i32 v[66:67], s[4:5], v66, s66, v[132:133]
	v_pk_add_f32 v[68:69], v[68:69], 1.0 op_sel_hi:[1,0]
	s_nop 0
	v_rcp_f32_e32 v62, v68
	v_rcp_f32_e32 v63, v69
	s_nop 0
	v_pk_mul_f32 v[58:59], v[62:63], v[58:59]
	v_pk_mul_f32 v[62:63], v[50:51], s[6:7] op_sel_hi:[1,0]
	v_pk_mul_f32 v[50:51], v[50:51], v[54:55]
	v_exp_f32_e32 v62, v62
	v_exp_f32_e32 v63, v63
	s_nop 0
	v_pk_add_f32 v[62:63], v[62:63], 1.0 op_sel_hi:[1,0]
	s_nop 0
	v_rcp_f32_e32 v54, v62
	v_rcp_f32_e32 v55, v63
	v_lshl_add_u64 v[62:63], v[66:67], 0, v[114:115]
	v_pk_mul_f32 v[54:55], v[54:55], v[50:51]
	v_pk_mul_f32 v[50:51], v[52:53], s[6:7] op_sel_hi:[1,0]
	s_nop 0
	v_exp_f32_e32 v50, v50
	v_exp_f32_e32 v51, v51
	s_nop 0
	v_pk_add_f32 v[50:51], v[50:51], 1.0 op_sel_hi:[1,0]
	s_nop 0
	v_rcp_f32_e32 v50, v50
	v_rcp_f32_e32 v51, v51
	s_nop 0
	v_pk_mul_f32 v[56:57], v[50:51], v[56:57]
	v_cvt_pk_bf16_f32 v50, v58, v59
	v_cvt_pk_bf16_f32 v51, v60, v61
	v_cvt_pk_bf16_f32 v52, v54, v55
	s_nop 0
	v_cvt_pk_bf16_f32 v53, v56, v57
	global_store_dwordx4 v[62:63], v[50:53], off
	s_nop 1
	v_pk_mul_f32 v[52:53], v[42:43], s[6:7] op_sel_hi:[1,0]
	v_pk_mul_f32 v[42:43], v[42:43], v[46:47]
	v_exp_f32_e32 v52, v52
	v_exp_f32_e32 v53, v53
	v_add_u32_e32 v50, 0x90, v131
	v_mad_i64_i32 v[50:51], s[4:5], v50, s66, v[132:133]
	v_pk_add_f32 v[52:53], v[52:53], 1.0 op_sel_hi:[1,0]
	s_nop 0
	v_rcp_f32_e32 v46, v52
	v_rcp_f32_e32 v47, v53
	s_nop 0
	v_pk_mul_f32 v[42:43], v[46:47], v[42:43]
	v_pk_mul_f32 v[46:47], v[34:35], s[6:7] op_sel_hi:[1,0]
	v_pk_mul_f32 v[34:35], v[34:35], v[38:39]
	v_exp_f32_e32 v46, v46
	v_exp_f32_e32 v47, v47
	s_nop 0
	v_pk_add_f32 v[46:47], v[46:47], 1.0 op_sel_hi:[1,0]
	s_nop 0
	v_rcp_f32_e32 v38, v46
	v_rcp_f32_e32 v39, v47
	v_lshl_add_u64 v[46:47], v[50:51], 0, v[114:115]
	v_pk_mul_f32 v[38:39], v[38:39], v[34:35]
	v_pk_mul_f32 v[34:35], v[36:37], s[6:7] op_sel_hi:[1,0]
	s_nop 0
	v_exp_f32_e32 v34, v34
	v_exp_f32_e32 v35, v35
	s_nop 0
	v_pk_add_f32 v[34:35], v[34:35], 1.0 op_sel_hi:[1,0]
	s_nop 0
	v_rcp_f32_e32 v34, v34
	v_rcp_f32_e32 v35, v35
	s_nop 0
	v_pk_mul_f32 v[40:41], v[34:35], v[40:41]
	v_cvt_pk_bf16_f32 v34, v42, v43
	v_cvt_pk_bf16_f32 v35, v44, v45
	v_cvt_pk_bf16_f32 v36, v38, v39
	s_nop 0
	v_cvt_pk_bf16_f32 v37, v40, v41
	global_store_dwordx4 v[46:47], v[34:37], off
	s_nop 1
	v_pk_mul_f32 v[36:37], v[26:27], s[6:7] op_sel_hi:[1,0]
; __device__ __forceinline__ unsigned cvt_pk_bf16(float lo, float hi) { unsigned r; asm volatile("v_cvt_pk_bf16_f32 %0, %1, %2" : "=v"(r) : "v"(lo), "v"(hi)); return r; }
; #define GAS __attribute__((address_space(1)))
;     __device__ __forceinline__ void operator()(const f32x4 (&acc)[2][2][4][2], const Unit& u, int wr, int wc, int fr, int fq) const {
;     ...
;                         const f32x2 g = {acc[ai][0][m][n][e], acc[ai][0][m][n][e + 1]}, up = {acc[ai][1][m][n][e], acc[ai][1][m][n][e + 1]};
;                         const f32x2 x = g * (f32x2){-1.44269504f, -1.44269504f};
;                         const f32x2 d = (f32x2){__builtin_amdgcn_exp2f(x.x), __builtin_amdgcn_exp2f(x.y)} + (f32x2){1.f, 1.f};
;                         const f32x2 o = (g * up) * (f32x2){__builtin_amdgcn_rcpf(d.x), __builtin_amdgcn_rcpf(d.y)};
;                         a[4 * n + e] = o.x; a[4 * n + e + 1] = o.y; }
;                 u32x4 w; w.x = cvt_pk_bf16(a[0], a[1]); w.y = cvt_pk_bf16(a[2], a[3]); w.z = cvt_pk_bf16(a[4], a[5]); w.w = cvt_pk_bf16(a[6], a[7]);
;                 *(u32x4*)rowp = w; }
; __device__ __forceinline__ void conv_load(const float* W, int N, int k0, int n0, int wave, int lane, f32x4 (&r)[8]) {
;     const int n = n0 + 4 * lane; const bool ok = n < N;
;     const float* p = W + (size_t)(k0 + 8 * wave) * N + n;
; #pragma unroll
;     for (int i = 0; i < 8; ++i) r[i] = ok ? __builtin_nontemporal_load((const GAS f32x4*)(p + (size_t)i * N)) : (f32x4){0.f, 0.f, 0.f, 0.f};
	v_pk_mul_f32 v[26:27], v[26:27], v[30:31]
	v_exp_f32_e32 v36, v36
	v_exp_f32_e32 v37, v37
	v_add_u32_e32 v34, 0xa0, v131
	v_mad_i64_i32 v[34:35], s[4:5], v34, s66, v[132:133]
	v_pk_add_f32 v[36:37], v[36:37], 1.0 op_sel_hi:[1,0]
	s_nop 0
	v_rcp_f32_e32 v30, v36
	v_rcp_f32_e32 v31, v37
	s_nop 0
	v_pk_mul_f32 v[26:27], v[30:31], v[26:27]
	v_pk_mul_f32 v[30:31], v[18:19], s[6:7] op_sel_hi:[1,0]
	v_pk_mul_f32 v[18:19], v[18:19], v[22:23]
	v_exp_f32_e32 v30, v30
	v_exp_f32_e32 v31, v31
	s_nop 0
	v_pk_add_f32 v[30:31], v[30:31], 1.0 op_sel_hi:[1,0]
	s_nop 0
	v_rcp_f32_e32 v22, v30
	v_rcp_f32_e32 v23, v31
	v_lshl_add_u64 v[30:31], v[34:35], 0, v[114:115]
	v_pk_mul_f32 v[22:23], v[22:23], v[18:19]
	v_pk_mul_f32 v[18:19], v[20:21], s[6:7] op_sel_hi:[1,0]
	s_nop 0
	v_exp_f32_e32 v18, v18
	v_exp_f32_e32 v19, v19
	s_nop 0
	v_pk_add_f32 v[18:19], v[18:19], 1.0 op_sel_hi:[1,0]
	s_nop 0
	v_rcp_f32_e32 v18, v18
	v_rcp_f32_e32 v19, v19
	s_nop 0
	v_pk_mul_f32 v[24:25], v[18:19], v[24:25]
	v_cvt_pk_bf16_f32 v18, v26, v27
	v_cvt_pk_bf16_f32 v19, v28, v29
	v_cvt_pk_bf16_f32 v20, v22, v23
	s_nop 0
	v_cvt_pk_bf16_f32 v21, v24, v25
	global_store_dwordx4 v[30:31], v[18:21], off
	s_nop 1
	v_pk_mul_f32 v[20:21], v[10:11], s[6:7] op_sel_hi:[1,0]
	v_pk_mul_f32 v[10:11], v[10:11], v[14:15]
	v_exp_f32_e32 v20, v20
	v_exp_f32_e32 v21, v21
	v_add_u32_e32 v18, 0xb0, v131
	v_mad_i64_i32 v[18:19], s[4:5], v18, s66, v[132:133]
	v_pk_add_f32 v[20:21], v[20:21], 1.0 op_sel_hi:[1,0]
	s_nop 0
	v_rcp_f32_e32 v14, v20
	v_rcp_f32_e32 v15, v21
	s_nop 0
	v_pk_mul_f32 v[10:11], v[14:15], v[10:11]
	v_pk_mul_f32 v[14:15], v[2:3], s[6:7] op_sel_hi:[1,0]
	v_pk_mul_f32 v[2:3], v[2:3], v[6:7]
	v_exp_f32_e32 v14, v14
	v_exp_f32_e32 v15, v15
	s_nop 0
	v_pk_add_f32 v[14:15], v[14:15], 1.0 op_sel_hi:[1,0]
	s_nop 0
	v_rcp_f32_e32 v6, v14
	v_rcp_f32_e32 v7, v15
	v_lshl_add_u64 v[14:15], v[18:19], 0, v[114:115]
	v_pk_mul_f32 v[6:7], v[6:7], v[2:3]
	v_pk_mul_f32 v[2:3], v[4:5], s[6:7] op_sel_hi:[1,0]
	s_nop 0
	v_exp_f32_e32 v2, v2
	v_exp_f32_e32 v3, v3
	s_nop 0
	v_pk_add_f32 v[2:3], v[2:3], 1.0 op_sel_hi:[1,0]
	s_nop 0
	v_rcp_f32_e32 v2, v2
	v_rcp_f32_e32 v3, v3
	s_nop 0
	v_pk_mul_f32 v[8:9], v[2:3], v[8:9]
	v_cvt_pk_bf16_f32 v2, v10, v11
	v_cvt_pk_bf16_f32 v3, v12, v13
	v_cvt_pk_bf16_f32 v4, v6, v7
	s_nop 0
	v_cvt_pk_bf16_f32 v5, v8, v9
	global_store_dwordx4 v[14:15], v[2:5], off
	s_cbranch_scc1 .LBB0_2444
	v_readfirstlane_b32 s2, v154
	s_mov_b64 s[14:15], s[92:93]
	s_ashr_i32 s2, s2, 6
	s_add_u32 s4, s14, s75
	s_addc_u32 s5, s15, 0
	s_load_dwordx2 s[4:5], s[4:5], 0x0
	v_mov_b32_e32 v2, 0
	s_waitcnt lgkmcnt(0)
	s_add_u32 s4, s4, s77
	s_addc_u32 s5, s5, s76
	s_lshl_b32 s31, s2, 3
	s_add_i32 s6, s78, s31
	s_mul_hi_i32 s7, s6, 0x7000
	s_mulk_i32 s6, 0x7000
	s_add_u32 s4, s4, s6
	s_addc_u32 s5, s5, s7
	v_lshl_add_u64 v[26:27], v[142:143], 2, s[4:5]
	v_mov_b32_e32 v6, v2
	v_mov_b32_e32 v7, v2
	v_mov_b32_e32 v8, v2
	v_mov_b32_e32 v9, v2
	s_and_saveexec_b64 s[4:5], s[38:39]
	s_cbranch_execz .LBB0_2288
	v_add_co_u32_e32 v6, vcc, 0x7000, v26
	s_nop 1
	v_addc_co_u32_e32 v7, vcc, 0, v27, vcc
	global_load_dwordx4 v[2:5], v[26:27], off nt
	s_nop 0
	global_load_dwordx4 v[6:9], v[6:7], off nt
.LBB0_2288:
	s_or_b64 exec, exec, s[4:5]
	s_and_saveexec_b64 s[4:5], s[40:41]
	s_xor_b64 s[4:5], exec, s[4:5]
	s_or_saveexec_b64 s[4:5], s[4:5]
	v_mov_b32_e32 v10, 0
	v_mov_b32_e32 v11, v10
	v_mov_b32_e32 v14, v10
	v_mov_b32_e32 v15, v10
	s_xor_b64 exec, exec, s[4:5]
	s_cbranch_execz .LBB0_2290
	v_add_co_u32_e32 v10, vcc, 0xe000, v26
	s_nop 1
	v_addc_co_u32_e32 v11, vcc, 0, v27, vcc
	v_add_co_u32_e32 v14, vcc, 0x15000, v26
	s_nop 1
	v_addc_co_u32_e32 v15, vcc, 0, v27, vcc
	global_load_dwordx4 v[10:13], v[10:11], off nt
	s_nop 0
	global_load_dwordx4 v[14:17], v[14:15], off nt
.LBB0_2290:
	s_or_b64 exec, exec, s[4:5]
	s_and_saveexec_b64 s[4:5], s[40:41]
	s_xor_b64 s[4:5], exec, s[4:5]
	s_or_saveexec_b64 s[4:5], s[4:5]
	v_mov_b32_e32 v18, 0
	v_mov_b32_e32 v19, v18
	v_mov_b32_e32 v22, v18
	v_mov_b32_e32 v23, v18
	s_xor_b64 exec, exec, s[4:5]
	s_cbranch_execz .LBB0_2292
	v_add_co_u32_e32 v18, vcc, 0x1c000, v26
	s_nop 1
	v_addc_co_u32_e32 v19, vcc, 0, v27, vcc
	v_add_co_u32_e32 v22, vcc, 0x23000, v26
	s_nop 1
	v_addc_co_u32_e32 v23, vcc, 0, v27, vcc
	global_load_dwordx4 v[18:21], v[18:19], off nt
	s_nop 0
	global_load_dwordx4 v[22:25], v[22:23], off nt
.LBB0_2292:
	s_or_b64 exec, exec, s[4:5]
	s_and_saveexec_b64 s[4:5], s[40:41]
	s_xor_b64 s[4:5], exec, s[4:5]
	s_or_saveexec_b64 s[4:5], s[4:5]
	v_mov_b32_e32 v50, 0
	s_xor_b64 exec, exec, s[4:5]
	s_cbranch_execz .LBB0_2296
	v_add_co_u32_e32 v28, vcc, 0x2a000, v26
	s_nop 1
	v_addc_co_u32_e32 v29, vcc, 0, v27, vcc
	v_add_co_u32_e32 v26, vcc, 0x31000, v26
	s_nop 1
	v_addc_co_u32_e32 v27, vcc, 0, v27, vcc
	global_load_dwordx4 v[50:53], v[28:29], off nt
	global_load_dwordx4 v[54:57], v[26:27], off nt

; #define GAS __attribute__((address_space(1)))
; #define CV_LOAD(j, R) do { ConvTile c_; if (CV_VALID(j) && CV_DEC(CV_TILE(j), c_)) conv_load(c_.W, c_.N, c_.k0, c_.n0, wave, lane, R); } while (0)
; __device__ __forceinline__ void conv_load(const float* W, int N, int k0, int n0, int wave, int lane, f32x4 (&r)[8]) {
;     const int n = n0 + 4 * lane; const bool ok = n < N;
;     const float* p = W + (size_t)(k0 + 8 * wave) * N + n;
; #pragma unroll
;     for (int i = 0; i < 8; ++i) r[i] = ok ? __builtin_nontemporal_load((const GAS f32x4*)(p + (size_t)i * N)) : (f32x4){0.f, 0.f, 0.f, 0.f};
; template <int NSLOT, bool MOE> __device__ __forceinline__ void conv_burst(const ConvHook& h, int bid, PG8_LAS unsigned char* T_, int tid) {
;     ...
;         CV_LOAD(0, R0); CV_LOAD(1, R1); CV_LOAD(2, R2);
.LBB0_2302:
	s_or_b64 exec, exec, s[4:5]
	v_mov_b32_e32 v66, 0
	s_and_saveexec_b64 s[4:5], s[44:45]
	s_cbranch_execz .LBB0_2304
	v_lshl_add_u64 v[58:59], v[58:59], 0, s[22:23]
	v_lshl_add_u64 v[60:61], v[58:59], 0, s[28:29]
	global_load_dwordx4 v[66:69], v[58:59], off nt
	global_load_dwordx4 v[70:73], v[60:61], off nt

; #define GAS __attribute__((address_space(1)))
; #define CV_LOAD(j, R) do { ConvTile c_; if (CV_VALID(j) && CV_DEC(CV_TILE(j), c_)) conv_load(c_.W, c_.N, c_.k0, c_.n0, wave, lane, R); } while (0)
; __device__ __forceinline__ void conv_load(const float* W, int N, int k0, int n0, int wave, int lane, f32x4 (&r)[8]) {
;     const int n = n0 + 4 * lane; const bool ok = n < N;
;     const float* p = W + (size_t)(k0 + 8 * wave) * N + n;
; #pragma unroll
;     for (int i = 0; i < 8; ++i) r[i] = ok ? __builtin_nontemporal_load((const GAS f32x4*)(p + (size_t)i * N)) : (f32x4){0.f, 0.f, 0.f, 0.f};
; template <int NSLOT, bool MOE> __device__ __forceinline__ void conv_burst(const ConvHook& h, int bid, PG8_LAS unsigned char* T_, int tid) {
;     ...
;         CV_LOAD(0, R0); CV_LOAD(1, R1); CV_LOAD(2, R2);
.LBB0_2310:
	s_or_b64 exec, exec, s[4:5]
	s_and_saveexec_b64 s[4:5], s[42:43]
	s_cbranch_execz .LBB0_2312
	v_add_co_u32_e32 v92, vcc, 0x2a000, v90
	s_nop 1
	v_addc_co_u32_e32 v93, vcc, 0, v91, vcc
	v_add_co_u32_e32 v90, vcc, 0x31000, v90
	s_nop 1
	v_addc_co_u32_e32 v91, vcc, 0, v91, vcc
	global_load_dwordx4 v[102:105], v[92:93], off nt
	global_load_dwordx4 v[106:109], v[90:91], off nt

; #define GAS __attribute__((address_space(1)))
; #define CV_LOAD(j, R) do { ConvTile c_; if (CV_VALID(j) && CV_DEC(CV_TILE(j), c_)) conv_load(c_.W, c_.N, c_.k0, c_.n0, wave, lane, R); } while (0)
; #define CV_PROC(j, R) { ConvTile c_; if (!CV_VALID(j) || !CV_DEC(CV_TILE(j), c_)) break; if constexpr (MOE) conv_emit_moe(c_, R, T, tid, wave, lane); else conv_emit(c_, R, T, tid, wave, lane); }
; __device__ __forceinline__ void conv_load(const float* W, int N, int k0, int n0, int wave, int lane, f32x4 (&r)[8]) {
;     const int n = n0 + 4 * lane; const bool ok = n < N;
;     const float* p = W + (size_t)(k0 + 8 * wave) * N + n;
; #pragma unroll
;     for (int i = 0; i < 8; ++i) r[i] = ok ? __builtin_nontemporal_load((const GAS f32x4*)(p + (size_t)i * N)) : (f32x4){0.f, 0.f, 0.f, 0.f};
; template <int NSLOT, bool MOE> __device__ __forceinline__ void conv_burst(const ConvHook& h, int bid, PG8_LAS unsigned char* T_, int tid) {
;     ...
;             CV_LOAD(j + 3, R3); CV_PROC(j, R0)
.Lhw_fast_6:
.Lhw_done_6:
	v_or_b32_e32 v90, s26, v157
	s_add_u32 s6, s6, s54
	s_addc_u32 s7, s7, s55
	v_ashrrev_i32_e32 v91, 31, v90
	v_cmp_gt_i32_e32 vcc, s12, v90
	v_lshl_add_u64 v[132:133], v[90:91], 2, s[6:7]
	s_and_saveexec_b64 s[6:7], vcc
	s_cbranch_execz .LBB0_2323
	s_lshl_b32 s24, s12, 2
	v_lshl_add_u64 v[92:93], v[132:133], 0, s[24:25]
	global_load_dwordx4 v[94:97], v[132:133], off nt
	global_load_dwordx4 v[98:101], v[92:93], off nt
.LBB0_2323:
	s_or_b64 exec, exec, s[6:7]
	s_and_saveexec_b64 s[6:7], vcc
	v_readlane_b32 s33, v254, 20
	s_cbranch_execz .LBB0_2325
	s_lshl_b32 s24, s12, 3
	v_lshl_add_u64 v[90:91], v[132:133], 0, s[24:25]
	s_lshl_b32 s24, s12, 2
	v_lshl_add_u64 v[110:111], v[90:91], 0, s[24:25]
	global_load_dwordx4 v[90:93], v[90:91], off nt
	s_nop 0
	global_load_dwordx4 v[110:113], v[110:111], off nt
.LBB0_2325:
	s_or_b64 exec, exec, s[6:7]
	s_and_saveexec_b64 s[6:7], vcc
	s_cbranch_execz .LBB0_2327
	s_lshl_b32 s24, s12, 4
	v_lshl_add_u64 v[114:115], v[132:133], 0, s[24:25]
	s_lshl_b32 s24, s12, 2
	v_lshl_add_u64 v[118:119], v[114:115], 0, s[24:25]
	global_load_dwordx4 v[114:117], v[114:115], off nt
	s_nop 0
	global_load_dwordx4 v[118:121], v[118:119], off nt
.LBB0_2327:
	s_or_b64 exec, exec, s[6:7]
	s_and_saveexec_b64 s[6:7], vcc
	s_cbranch_execz .LBB0_2329
	s_mul_i32 s24, s12, 24
	v_lshl_add_u64 v[122:123], v[132:133], 0, s[24:25]
	s_lshl_b32 s24, s12, 2
	v_lshl_add_u64 v[124:125], v[122:123], 0, s[24:25]
	global_load_dwordx4 v[126:129], v[122:123], off nt
	s_nop 0
	global_load_dwordx4 v[122:125], v[124:125], off nt

; #define GAS __attribute__((address_space(1)))
; #define CV_LOAD(j, R) do { ConvTile c_; if (CV_VALID(j) && CV_DEC(CV_TILE(j), c_)) conv_load(c_.W, c_.N, c_.k0, c_.n0, wave, lane, R); } while (0)
; #define CV_PROC(j, R) { ConvTile c_; if (!CV_VALID(j) || !CV_DEC(CV_TILE(j), c_)) break; if constexpr (MOE) conv_emit_moe(c_, R, T, tid, wave, lane); else conv_emit(c_, R, T, tid, wave, lane); }
; __device__ __forceinline__ void conv_load(const float* W, int N, int k0, int n0, int wave, int lane, f32x4 (&r)[8]) {
;     const int n = n0 + 4 * lane; const bool ok = n < N;
;     const float* p = W + (size_t)(k0 + 8 * wave) * N + n;
; #pragma unroll
;     for (int i = 0; i < 8; ++i) r[i] = ok ? __builtin_nontemporal_load((const GAS f32x4*)(p + (size_t)i * N)) : (f32x4){0.f, 0.f, 0.f, 0.f};
; template <int NSLOT, bool MOE> __device__ __forceinline__ void conv_burst(const ConvHook& h, int bid, PG8_LAS unsigned char* T_, int tid) {
;     ...
;             CV_LOAD(j + 4, R0); CV_PROC(j + 1, R1)
.LBB0_2356:
	s_add_i32 s12, s24, s31
	s_mul_hi_i32 s13, s12, s26
	s_mul_i32 s12, s12, s26
	v_or_b32_e32 v2, s33, v157
	s_lshl_b64 s[12:13], s[12:13], 2
	v_cmp_le_i32_e32 vcc, s26, v2
	s_add_u32 s12, s6, s12
	s_addc_u32 s13, s7, s13
	s_and_saveexec_b64 s[6:7], vcc
	s_xor_b64 s[6:7], exec, s[6:7]
	s_or_saveexec_b64 s[6:7], s[6:7]
	v_ashrrev_i32_e32 v3, 31, v2
	v_lshl_add_u64 v[132:133], v[2:3], 2, s[12:13]
	s_xor_b64 exec, exec, s[6:7]
	s_cbranch_execz .LBB0_2358
	s_lshl_b32 s24, s26, 2
	v_lshl_add_u64 v[6:7], v[132:133], 0, s[24:25]
	global_load_dwordx4 v[2:5], v[132:133], off nt
	s_nop 0
	global_load_dwordx4 v[6:9], v[6:7], off nt
.LBB0_2358:
	s_or_b64 exec, exec, s[6:7]
	s_and_saveexec_b64 s[6:7], vcc
	s_xor_b64 s[6:7], exec, s[6:7]
	s_or_saveexec_b64 s[6:7], s[6:7]
	s_xor_b64 exec, exec, s[6:7]
	s_cbranch_execz .LBB0_2360
	s_lshl_b32 s24, s26, 3
	v_lshl_add_u64 v[10:11], v[132:133], 0, s[24:25]
	s_lshl_b32 s24, s26, 2
	v_lshl_add_u64 v[14:15], v[10:11], 0, s[24:25]
	global_load_dwordx4 v[10:13], v[10:11], off nt
	s_nop 0
	global_load_dwordx4 v[14:17], v[14:15], off nt
.LBB0_2360:
	s_or_b64 exec, exec, s[6:7]
	s_and_saveexec_b64 s[6:7], vcc
	s_xor_b64 s[6:7], exec, s[6:7]
	s_or_saveexec_b64 s[6:7], s[6:7]
	s_xor_b64 exec, exec, s[6:7]
	s_cbranch_execz .LBB0_2362
	s_lshl_b32 s24, s26, 4
	v_lshl_add_u64 v[18:19], v[132:133], 0, s[24:25]
	s_lshl_b32 s24, s26, 2
	v_lshl_add_u64 v[22:23], v[18:19], 0, s[24:25]
	global_load_dwordx4 v[18:21], v[18:19], off nt
	s_nop 0
	global_load_dwordx4 v[22:25], v[22:23], off nt
.LBB0_2362:
	s_or_b64 exec, exec, s[6:7]
	s_and_saveexec_b64 s[6:7], vcc
	s_xor_b64 s[6:7], exec, s[6:7]
	s_or_saveexec_b64 s[6:7], s[6:7]
	s_xor_b64 exec, exec, s[6:7]
	s_cbranch_execz .LBB0_2366
	s_mul_i32 s24, s26, 24
	v_lshl_add_u64 v[50:51], v[132:133], 0, s[24:25]
	s_lshl_b32 s24, s26, 2
	v_lshl_add_u64 v[54:55], v[50:51], 0, s[24:25]
	global_load_dwordx4 v[50:53], v[50:51], off nt
	s_nop 0
	global_load_dwordx4 v[54:57], v[54:55], off nt

; #define GAS __attribute__((address_space(1)))
; #define CV_LOAD(j, R) do { ConvTile c_; if (CV_VALID(j) && CV_DEC(CV_TILE(j), c_)) conv_load(c_.W, c_.N, c_.k0, c_.n0, wave, lane, R); } while (0)
; #define CV_PROC(j, R) { ConvTile c_; if (!CV_VALID(j) || !CV_DEC(CV_TILE(j), c_)) break; if constexpr (MOE) conv_emit_moe(c_, R, T, tid, wave, lane); else conv_emit(c_, R, T, tid, wave, lane); }
; __device__ __forceinline__ void conv_load(const float* W, int N, int k0, int n0, int wave, int lane, f32x4 (&r)[8]) {
;     const int n = n0 + 4 * lane; const bool ok = n < N;
;     const float* p = W + (size_t)(k0 + 8 * wave) * N + n;
; #pragma unroll
;     for (int i = 0; i < 8; ++i) r[i] = ok ? __builtin_nontemporal_load((const GAS f32x4*)(p + (size_t)i * N)) : (f32x4){0.f, 0.f, 0.f, 0.f};
; template <int NSLOT, bool MOE> __device__ __forceinline__ void conv_burst(const ConvHook& h, int bid, PG8_LAS unsigned char* T_, int tid) {
;     ...
;             CV_LOAD(j + 5, R1); CV_PROC(j + 2, R2)
.LBB0_2392:
	s_or_b64 exec, exec, s[6:7]
	s_and_saveexec_b64 s[6:7], vcc
	s_cbranch_execz .LBB0_2394
	s_mul_i32 s24, s12, 24
	v_lshl_add_u64 v[66:67], v[152:153], 0, s[24:25]
	s_lshl_b32 s24, s12, 2
	v_lshl_add_u64 v[70:71], v[66:67], 0, s[24:25]
	global_load_dwordx4 v[66:69], v[66:67], off nt
	s_nop 0
	global_load_dwordx4 v[70:73], v[70:71], off nt

; #define GAS __attribute__((address_space(1)))
; #define CV_LOAD(j, R) do { ConvTile c_; if (CV_VALID(j) && CV_DEC(CV_TILE(j), c_)) conv_load(c_.W, c_.N, c_.k0, c_.n0, wave, lane, R); } while (0)
; #define CV_PROC(j, R) { ConvTile c_; if (!CV_VALID(j) || !CV_DEC(CV_TILE(j), c_)) break; if constexpr (MOE) conv_emit_moe(c_, R, T, tid, wave, lane); else conv_emit(c_, R, T, tid, wave, lane); }
; __device__ __forceinline__ void conv_load(const float* W, int N, int k0, int n0, int wave, int lane, f32x4 (&r)[8]) {
;     const int n = n0 + 4 * lane; const bool ok = n < N;
;     const float* p = W + (size_t)(k0 + 8 * wave) * N + n;
; #pragma unroll
;     for (int i = 0; i < 8; ++i) r[i] = ok ? __builtin_nontemporal_load((const GAS f32x4*)(p + (size_t)i * N)) : (f32x4){0.f, 0.f, 0.f, 0.f};
; template <int NSLOT, bool MOE> __device__ __forceinline__ void conv_burst(const ConvHook& h, int bid, PG8_LAS unsigned char* T_, int tid) {
;     ...
;             CV_LOAD(j + 6, R2); CV_PROC(j + 3, R3)
.LBB0_2424:
	s_or_b64 exec, exec, s[6:7]
	s_and_saveexec_b64 s[6:7], vcc
	s_cbranch_execz .LBB0_2426
	s_mul_i32 s24, s12, 24
	v_lshl_add_u64 v[102:103], v[152:153], 0, s[24:25]
	s_lshl_b32 s24, s12, 2
	v_lshl_add_u64 v[106:107], v[102:103], 0, s[24:25]
	global_load_dwordx4 v[102:105], v[102:103], off nt
	s_nop 0
	global_load_dwordx4 v[106:109], v[106:107], off nt
